# v10 plus GEMM phase prologue: second batch of stage loads issued before the first wait (vmcnt(8) then vmcnt(6))
# baseline (speedup 1.0000x reference)
.LBB0_291:
	s_lshl_b64 s[20:21], s[38:39], 6
	s_mul_i32 s25, s38, 0x840
	s_mul_hi_i32 s24, s38, 0x840
	s_add_u32 s58, s85, s25
	v_readlane_b32 s25, v255, 46
	s_addc_u32 s59, s25, s24
	s_add_u32 s60, s58, s20
	s_addc_u32 s61, s59, s21
	s_lshl_b32 s26, s26, 9
	s_lshl_b64 s[20:21], s[26:27], 2
	s_add_u32 s20, s40, s20
	s_addc_u32 s21, s41, s21
	s_add_u32 s20, s20, 0x18420000
	s_addc_u32 s21, s21, 0
	v_writelane_b32 v255, s20, 50
	v_lshl_add_u64 v[8:9], v[8:9], 0, s[34:35]
	v_writelane_b32 v255, s21, 51
	s_mul_i32 s21, s38, 0x2400
	s_mul_hi_i32 s20, s38, 0x2400
	s_add_u32 s40, s60, s21
	s_addc_u32 s41, s61, s20
	s_mul_i32 s21, s38, 0x1800
	s_mul_hi_i32 s20, s38, 0x1800
	s_add_u32 s24, s40, s21
	s_addc_u32 s25, s41, s20
	s_lshl_b64 s[20:21], s[38:39], 8
	s_add_u32 s24, s24, s20
	s_addc_u32 s25, s25, s21
	s_add_i32 m0, s94, 0x18000
	v_lshl_add_u64 v[4:5], v[4:5], 0, s[34:35]
	global_load_lds_dwordx4 v[8:9], off
	s_add_i32 m0, s94, 0x1a000
	s_add_i32 s26, s94, 0x8000
	global_load_lds_dwordx4 v[4:5], off
	v_lshl_add_u64 v[4:5], v[6:7], 0, s[34:35]
	s_mov_b32 m0, s26
	s_add_i32 s56, s94, 0xa000
	global_load_lds_dwordx4 v[4:5], off
	v_lshl_add_u64 v[4:5], v[10:11], 0, s[34:35]
	s_mov_b32 m0, s56
	v_lshl_add_u64 v[2:3], v[2:3], 0, s[34:35]
	global_load_lds_dwordx4 v[4:5], off
	s_add_i32 m0, s94, 0x1c000
	v_lshl_add_u64 v[0:1], v[0:1], 0, s[34:35]
	global_load_lds_dwordx4 v[2:3], off
	s_add_i32 m0, s94, 0x1e000
	s_lshr_b32 s9, s9, 26
	global_load_lds_dwordx4 v[0:1], off
	v_bfe_u32 v1, v12, 4, 2
	v_and_b32_e32 v0, 15, v12
	s_add_i32 s9, s8, s9
	v_lshlrev_b32_e32 v2, 3, v1
	v_lshlrev_b32_e32 v1, 4, v1
	v_lshlrev_b32_e32 v4, 2, v12
	s_and_b32 s57, s17, 3
	s_ashr_i32 s91, s9, 6
	v_lshl_or_b32 v3, v0, 6, v1
	s_lshl_b32 s9, s18, 13
	v_and_b32_e32 v4, 32, v4
	v_bitop3_b32 v5, v3, s9, v4 bitop3:0xde
	s_lshl_b32 s9, s57, 12
	s_cmp_gt_i32 s8, 63
	s_cselect_b64 s[64:65], -1, 0
	s_or_b32 s92, s57, 16
	s_or_b32 s20, s57, 20
	s_add_i32 s21, s91, -2
	s_cmpk_lt_u32 s1, 0x100
	s_cselect_b64 s[66:67], -1, 0
	s_and_b32 s1, s1, 0x1fffff00
	s_lshl_b32 s8, s57, 6
	s_or_b32 s1, s8, s1
	v_lshl_or_b32 v49, s18, 6, v0
	v_or3_b32 v0, s1, v1, v0
	v_lshlrev_b32_e32 v0, 3, v0
	s_cmp_lt_u32 s57, 2
	v_ashrrev_i32_e32 v1, 31, v0
	s_cselect_b64 s[68:69], -1, 0
	s_ashr_i32 s1, s50, 31
	v_lshl_add_u64 v[182:183], v[0:1], 1, s[40:41]
	s_lshr_b32 s1, s1, 29
	v_add_u32_e32 v0, v16, v13
	s_add_i32 s1, s50, s1
	v_add_lshl_u32 v0, v0, v15, 1
	v_mov_b32_e32 v1, v48
	s_waitcnt vmcnt(8)
	s_barrier
	s_waitcnt vmcnt(6)
	s_ashr_i32 s8, s1, 3
	s_and_b32 s1, s1, -8
	v_lshl_add_u64 v[186:187], s[52:53], 0, v[0:1]
	v_add_u32_e32 v0, v19, v17
	v_bitop3_b32 v218, v3, s9, v4 bitop3:0xde
	v_lshl_or_b32 v219, s57, 5, v2
	v_and_b32_e32 v2, 0x3f0, v14
	v_mov_b32_e32 v3, v48
	s_sub_i32 s17, s50, s1
	v_writelane_b32 v255, s8, 52
	s_add_i32 s1, s8, 1
	v_add_lshl_u32 v0, v0, v18, 1
	s_lshl_b32 s89, s18, 3
	s_add_i32 s90, s57, 2
	s_add_i32 s62, s57, 6
	s_add_i32 s63, s57, 18
	s_add_i32 s88, s57, 22
	v_lshl_add_u64 v[184:185], s[24:25], 0, v[2:3]
	v_writelane_b32 v255, s1, 53
	v_lshl_add_u64 v[188:189], s[52:53], 0, v[0:1]
	s_mov_b32 s18, 0
	v_add_u32_e32 v220, 0, v5
	s_barrier
	s_branch .LBB0_294

.LBB0_979:
	s_mul_i32 s38, s40, 0xc00
	s_mul_hi_i32 s30, s40, 0xc00
	s_add_u32 s52, s1, s38
	s_addc_u32 s53, s5, s30
	s_mul_i32 s38, s40, 0xffffe680
	s_mul_hi_i32 s30, s40, 0xffffe680
	s_add_u32 s38, s1, s38
	s_addc_u32 s39, s5, s30
	s_add_i32 m0, s21, 0x18000
	v_lshl_add_u64 v[0:1], v[0:1], 0, s[34:35]
	global_load_lds_dwordx4 v[0:1], off
	v_lshl_add_u64 v[0:1], v[2:3], 0, s[34:35]
	s_add_i32 m0, s21, 0x1a000
	s_add_i32 s64, s21, 0x8000
	global_load_lds_dwordx4 v[0:1], off
	v_lshl_add_u64 v[0:1], v[8:9], 0, s[34:35]
	s_mov_b32 m0, s64
	s_add_i32 s65, s21, 0xa000
	global_load_lds_dwordx4 v[0:1], off
	v_lshl_add_u64 v[0:1], v[10:11], 0, s[34:35]
	s_mov_b32 m0, s65
	v_bfe_u32 v20, v15, 4, 2
	global_load_lds_dwordx4 v[0:1], off
	s_add_i32 m0, s21, 0x1c000
	v_lshl_add_u64 v[0:1], v[4:5], 0, s[34:35]
	global_load_lds_dwordx4 v[0:1], off
	v_lshl_add_u64 v[0:1], v[6:7], 0, s[34:35]
	s_add_i32 m0, s21, 0x1e000
	v_and_b32_e32 v19, 15, v15
	global_load_lds_dwordx4 v[0:1], off
	s_lshr_b32 s30, s43, 26
	v_lshlrev_b32_e32 v21, 3, v20
	v_lshlrev_b32_e32 v20, 4, v20
	v_lshlrev_b32_e32 v15, 2, v15
	s_and_b32 s28, s28, 3
	s_add_i32 s30, s42, s30
	v_lshl_or_b32 v49, s29, 6, v19
	v_lshl_or_b32 v22, v19, 6, v20
	s_lshl_b32 s29, s29, 13
	v_and_b32_e32 v15, 32, v15
	s_ashr_i32 s63, s30, 6
	v_bitop3_b32 v23, v22, s29, v15 bitop3:0xde
	s_lshl_b32 s29, s28, 12
	s_cmp_gt_i32 s42, 63
	s_cselect_b64 s[54:55], -1, 0
	s_add_i32 s66, s63, -2
	s_cmpk_lt_u32 s25, 0x100
	v_lshl_or_b32 v217, s28, 5, v21
	s_cselect_b64 s[56:57], -1, 0
	s_and_b32 s25, s25, 0x1fffff00
	s_lshl_b32 s28, s28, 6
	s_or_b32 s25, s28, s25
	v_or3_b32 v0, s25, v20, v19
	v_lshlrev_b32_e32 v0, 3, v0
	v_ashrrev_i32_e32 v1, 31, v0
	v_lshlrev_b64 v[0:1], 1, v[0:1]
	v_bitop3_b32 v216, v22, s29, v15 bitop3:0xde
	v_lshl_add_u64 v[202:203], s[38:39], 0, v[0:1]
	v_lshl_add_u64 v[0:1], s[58:59], 0, v[0:1]
	s_mov_b64 s[28:29], 0x18422000
	v_lshl_add_u64 v[204:205], v[0:1], 0, s[28:29]
	s_lshr_b32 s28, s41, 23
	s_add_i32 s28, s40, s28
	v_add_u32_e32 v0, v14, v12
	s_lshl_b32 s25, s4, 2
	s_ashr_i32 s67, s28, 9
	s_lshr_b32 s28, s4, 29
	v_add_lshl_u32 v0, v0, v13, 1
	v_mov_b32_e32 v1, v48
	s_waitcnt vmcnt(8)
	s_barrier
	s_waitcnt vmcnt(6)
	s_add_i32 s28, s25, s28
	v_lshl_add_u64 v[206:207], s[46:47], 0, v[0:1]
	v_add_u32_e32 v0, v18, v16
	s_and_b32 s28, s28, -8
	v_add_lshl_u32 v0, v0, v17, 1
	s_sub_i32 s68, s25, s28
	s_add_i32 s69, s67, 1
	v_lshl_add_u64 v[208:209], s[46:47], 0, v[0:1]
	s_mov_b32 s70, 0
	v_add_u32_e32 v218, 0, v23
	s_barrier
	s_branch .LBB0_982

.LBB0_1098:
	s_add_u32 s60, s40, 0x18422000
	s_addc_u32 s61, s41, 0
	s_add_i32 m0, s69, 0x18000
	v_lshl_add_u64 v[0:1], v[0:1], 0, s[34:35]
	global_load_lds_dwordx4 v[0:1], off
	v_lshl_add_u64 v[0:1], v[2:3], 0, s[34:35]
	s_add_i32 m0, s69, 0x1a000
	s_add_i32 s79, s69, 0x8000
	global_load_lds_dwordx4 v[0:1], off
	v_lshl_add_u64 v[0:1], v[8:9], 0, s[34:35]
	s_mov_b32 m0, s79
	s_add_i32 s88, s69, 0xa000
	global_load_lds_dwordx4 v[0:1], off
	v_lshl_add_u64 v[0:1], v[10:11], 0, s[34:35]
	s_mov_b32 m0, s88
	v_bfe_u32 v19, v18, 4, 2
	global_load_lds_dwordx4 v[0:1], off
	s_add_i32 m0, s69, 0x1c000
	v_lshl_add_u64 v[0:1], v[4:5], 0, s[34:35]
	global_load_lds_dwordx4 v[0:1], off
	v_lshl_add_u64 v[0:1], v[6:7], 0, s[34:35]
	s_add_i32 m0, s69, 0x1e000
	s_lshr_b32 s39, s39, 26
	global_load_lds_dwordx4 v[0:1], off
	v_lshlrev_b32_e32 v0, 2, v234
	v_and_b32_e32 v0, 60, v0
	v_lshrrev_b32_e32 v1, 4, v234
	v_add_lshl_u32 v181, v0, v1, 2
	v_lshlrev_b32_e32 v0, 3, v234
	v_and_b32_e32 v1, 64, v234
	v_and_b32_e32 v49, 15, v18
	s_add_i32 s39, s38, s39
	v_lshlrev_b32_e32 v20, 4, v19
	v_lshlrev_b32_e32 v18, 2, v18
	v_and_b32_e32 v182, 24, v0
	v_xor_b32_e32 v0, 16, v234
	v_add_u32_e32 v1, 64, v1
	s_and_b32 s40, s42, 3
	s_ashr_i32 s70, s39, 6
	v_lshl_or_b32 v21, v49, 6, v20
	s_lshl_b32 s39, s30, 13
	v_and_b32_e32 v18, 32, v18
	v_cmp_lt_i32_e32 vcc, v0, v1
	s_lshl_b32 s71, s30, 6
	v_bitop3_b32 v22, v21, s39, v18 bitop3:0xde
	s_lshl_b32 s78, s40, 5
	s_lshl_b32 s39, s40, 12
	v_cndmask_b32_e32 v0, v234, v0, vcc
	s_cmp_gt_i32 s38, 63
	v_lshlrev_b32_e32 v183, 2, v0
	v_xor_b32_e32 v0, 32, v234
	s_cselect_b64 s[62:63], -1, 0
	s_add_i32 s89, s70, -2
	v_cmp_lt_i32_e32 vcc, v0, v1
	s_cmpk_lt_u32 s29, 0x100
	s_cselect_b64 s[64:65], -1, 0
	v_cndmask_b32_e32 v0, v234, v0, vcc
	v_lshlrev_b32_e32 v184, 2, v0
	s_lshl_b32 s41, s40, 2
	s_and_b32 s29, s29, 0xffffff00
	s_lshl_b32 s40, s40, 6
	v_add_u32_e32 v0, v14, v12
	s_lshl_b32 s30, s30, 10
	s_or_b32 s29, s40, s29
	v_add_lshl_u32 v0, v0, v13, 1
	v_mov_b32_e32 v1, v48
	s_waitcnt vmcnt(8)
	s_barrier
	s_waitcnt vmcnt(6)
	s_or_b32 s30, s41, s30
	v_or3_b32 v185, s29, v20, v49
	v_lshl_add_u64 v[166:167], s[52:53], 0, v[0:1]
	v_add_u32_e32 v0, v17, v15
	v_lshlrev_b32_e32 v2, 4, v49
	s_add_i32 s30, s30, 0x22400
	s_movk_i32 s29, 0x100
	v_lshlrev_b32_e32 v3, 4, v185
	v_add_lshl_u32 v0, v0, v16, 1
	v_lshlrev_b32_e32 v178, 3, v19
	v_bitop3_b32 v179, v21, s39, v18 bitop3:0xde
	v_lshrrev_b32_e32 v180, 2, v234
	s_mov_b32 s90, 0
	v_cmp_eq_u32_e64 s[38:39], 0, v19
	v_cmp_gt_i32_e64 s[40:41], s29, v185
	v_lshl_add_u64 v[168:169], s[52:53], 0, v[0:1]
	v_add_u32_e32 v186, 0, v22
	v_add_u32_e32 v187, s30, v2
	v_add_u32_e32 v188, 0x22400, v3
	s_barrier
	s_branch .LBB0_1101

.LBB0_1349:
	s_lshl_b64 s[8:9], s[8:9], 4
	s_add_u32 s58, s6, s19
	s_addc_u32 s59, s7, s28
	s_add_u32 s8, s50, s8
	s_addc_u32 s9, s51, s9
	s_add_u32 s64, s8, 0x8000
	v_lshrrev_b32_e32 v10, 1, v2
	s_addc_u32 s65, s9, 0
	s_lshr_b32 s5, s5, 26
	v_and_b32_e32 v10, 24, v10
	v_and_b32_e32 v3, 15, v2
	s_add_i32 s5, s4, s5
	v_lshlrev_b32_e32 v11, 1, v10
	v_lshlrev_b32_e32 v2, 2, v2
	s_ashr_i32 s19, s5, 6
	v_lshl_or_b32 v160, s25, 6, v3
	v_lshl_or_b32 v3, v3, 6, v11
	s_lshl_b32 s5, s25, 13
	v_and_b32_e32 v2, 32, v2
	v_bitop3_b32 v11, v3, s5, v2 bitop3:0xde
	s_lshl_b32 s5, s29, 5
	v_mov_b32_e32 v131, v48
	s_and_b32 s8, s5, 0x60
	v_lshl_add_u64 v[4:5], v[144:145], 0, v[130:131]
	s_lshl_b32 s5, s8, 7
	v_bitop3_b32 v161, v3, s5, v2 bitop3:0xde
	s_add_i32 m0, s38, 0x18000
	v_lshl_add_u64 v[2:3], v[4:5], 0, s[34:35]
	v_mov_b32_e32 v133, v48
	global_load_lds_dwordx4 v[2:3], off
	s_add_i32 m0, s38, 0x1a000
	v_lshl_add_u64 v[6:7], v[144:145], 0, v[132:133]
	s_add_u32 s66, s6, 0x18422080
	v_mov_b32_e32 v137, v48
	v_lshl_add_u64 v[2:3], v[6:7], 0, s[34:35]
	s_addc_u32 s67, s7, 0
	s_add_i32 s61, s38, 0x8000
	v_mov_b32_e32 v139, v48
	global_load_lds_dwordx4 v[2:3], off
	v_lshl_add_u64 v[2:3], s[66:67], 0, v[136:137]
	s_mov_b32 m0, s61
	s_add_i32 s25, s38, 0xa000
	v_lshl_add_u64 v[8:9], v[0:1], 0, v[130:131]
	global_load_lds_dwordx4 v[2:3], off
	v_lshl_add_u64 v[2:3], s[66:67], 0, v[138:139]
	s_mov_b32 m0, s25
	v_lshl_add_u64 v[0:1], v[0:1], 0, v[132:133]
	global_load_lds_dwordx4 v[2:3], off
	s_add_i32 m0, s38, 0x1c000
	v_lshl_add_u64 v[2:3], v[8:9], 0, s[34:35]
	global_load_lds_dwordx4 v[2:3], off
	v_lshl_add_u64 v[0:1], v[0:1], 0, s[34:35]
	s_add_i32 m0, s38, 0x1e000
	s_cmp_gt_i32 s4, 63
	global_load_lds_dwordx4 v[0:1], off
	s_waitcnt vmcnt(8)
	s_barrier
	s_waitcnt vmcnt(6)
	s_cselect_b64 s[68:69], -1, 0
	s_add_i32 s5, s19, -2
	s_cmpk_lt_u32 s12, 0x100
	s_cselect_b64 s[70:71], -1, 0
	v_or_b32_e32 v137, s8, v10
	s_mov_b32 s12, 0
	v_mov_b32_e32 v146, s40
	v_mov_b32_e32 v158, s30
	v_add_u32_e32 v139, 0, v11
	s_barrier
	s_branch .LBB0_1352

.LBB0_1433:
	s_mul_i32 s58, s8, 0x4980
	s_mul_hi_i32 s59, s8, 0x4980
	s_add_u32 s30, s30, s58
	s_addc_u32 s40, s40, s59
	s_lshl_b64 s[66:67], s[8:9], 3
	s_add_u32 s56, s6, 0x18422000
	s_addc_u32 s57, s7, 0
	s_add_u32 s58, s5, s58
	s_mul_hi_i32 s9, s8, 0xa14
	s_mulk_i32 s8, 0xa14
	s_addc_u32 s59, s12, s59
	s_add_u32 s6, s6, s8
	s_addc_u32 s7, s7, s9
	s_add_u32 s64, s6, s30
	s_addc_u32 s65, s7, s40
	s_add_u32 s6, s64, s66
	v_mov_b32_e32 v157, v48
	s_addc_u32 s7, s65, s67
	v_lshl_add_u64 v[14:15], v[130:131], 0, v[156:157]
	v_mov_b32_e32 v161, v48
	s_add_u32 s66, s6, 0x4000
	v_lshl_add_u64 v[16:17], v[130:131], 0, v[160:161]
	s_addc_u32 s67, s7, 0
	s_add_i32 m0, s25, 0x18000
	v_lshl_add_u64 v[14:15], v[14:15], 0, s[34:35]
	global_load_lds_dwordx4 v[14:15], off
	v_lshl_add_u64 v[14:15], v[16:17], 0, s[34:35]
	s_add_i32 m0, s25, 0x1a000
	s_add_i32 s96, s25, 0x8000
	global_load_lds_dwordx4 v[14:15], off
	v_lshl_add_u64 v[0:1], v[0:1], 0, s[34:35]
	s_mov_b32 m0, s96
	s_add_i32 s97, s25, 0xa000
	v_lshl_add_u64 v[18:19], v[4:5], 0, v[156:157]
	global_load_lds_dwordx4 v[0:1], off
	v_lshl_add_u64 v[0:1], v[2:3], 0, s[34:35]
	s_mov_b32 m0, s97
	v_lshl_add_u64 v[4:5], v[4:5], 0, v[160:161]
	global_load_lds_dwordx4 v[0:1], off
	s_add_i32 m0, s25, 0x1c000
	v_lshl_add_u64 v[0:1], v[18:19], 0, s[34:35]
	global_load_lds_dwordx4 v[0:1], off
	v_lshl_add_u64 v[0:1], v[4:5], 0, s[34:35]
	s_add_i32 m0, s25, 0x1e000
	v_lshrrev_b32_e32 v13, 1, v6
	global_load_lds_dwordx4 v[0:1], off
	s_lshr_b32 s6, s43, 26
	v_and_b32_e32 v201, 24, v13
	v_and_b32_e32 v49, 15, v6
	s_add_i32 s6, s42, s6
	v_lshlrev_b32_e32 v13, 1, v201
	v_lshlrev_b32_e32 v6, 2, v6
	s_ashr_i32 s30, s6, 6
	v_lshl_or_b32 v13, v49, 6, v13
	s_lshl_b32 s6, s29, 13
	v_and_b32_e32 v6, 32, v6
	v_bitop3_b32 v20, v13, s6, v6 bitop3:0xde
	s_lshl_b32 s6, s41, 5
	s_and_b32 s95, s6, 0x60
	s_lshl_b32 s94, s29, 6
	s_lshl_b32 s6, s95, 7
	s_cmp_gt_i32 s42, 63
	s_cselect_b64 s[68:69], -1, 0
	s_add_i32 s93, s30, -2
	s_cmpk_lt_u32 s28, 0x100
	v_lshlrev_b32_e32 v0, 2, v234
	s_cselect_b64 s[70:71], -1, 0
	v_and_b32_e32 v0, 60, v0
	v_lshrrev_b32_e32 v1, 4, v234
	s_lshr_b32 s7, s4, 31
	v_add_lshl_u32 v206, v0, v1, 2
	v_lshlrev_b32_e32 v0, 3, v234
	s_add_i32 s7, s4, s7
	v_and_b32_e32 v207, 24, v0
	s_ashr_i32 s8, s7, 1
	s_bfe_i32 s7, s4, 0x1001d
	v_add_u32_e32 v0, v9, v7
	v_bitop3_b32 v203, v13, s6, v6 bitop3:0xde
	s_lshl_b32 s6, s4, 2
	s_lshr_b32 s7, s7, 29
	v_add_lshl_u32 v0, v0, v8, 1
	v_mov_b32_e32 v1, v48
	s_waitcnt vmcnt(8)
	s_barrier
	s_waitcnt vmcnt(6)
	s_add_i32 s7, s6, s7
	v_lshl_add_u64 v[162:163], s[50:51], 0, v[0:1]
	v_add_u32_e32 v0, v12, v10
	s_and_b32 s7, s7, -8
	v_add_lshl_u32 v0, v0, v11, 1
	v_lshrrev_b32_e32 v205, 2, v234
	s_sub_i32 s28, s6, s7
	v_writelane_b32 v255, s8, 38
	s_add_i32 s29, s8, 1
	v_lshl_add_u64 v[164:165], s[50:51], 0, v[0:1]
	s_mov_b32 s82, 0
	v_add_u32_e32 v208, 0, v20
	s_barrier
	s_branch .LBB0_1436

.LBB0_1554:
	s_lshl_b64 s[52:53], s[40:41], 12
	s_lshl_b64 s[40:41], s[40:41], 7
	s_add_u32 s25, s50, s52
	s_addc_u32 s51, s51, s53
	s_add_u32 s50, s25, 0x18422000
	v_lshrrev_b32_e32 v20, 1, v18
	s_addc_u32 s51, s51, 0
	v_and_b32_e32 v20, 24, v20
	s_add_u32 s52, s50, s40
	v_and_b32_e32 v19, 15, v18
	v_lshlrev_b32_e32 v21, 1, v20
	v_lshlrev_b32_e32 v18, 2, v18
	s_addc_u32 s53, s51, s41
	v_lshl_or_b32 v49, s12, 6, v19
	v_lshl_or_b32 v19, v19, 6, v21
	s_lshl_b32 s12, s12, 13
	v_and_b32_e32 v18, 32, v18
	v_bitop3_b32 v21, v19, s12, v18 bitop3:0xde
	s_lshl_b32 s12, s19, 5
	s_lshr_b32 s25, s39, 26
	s_and_b32 s39, s12, 0x60
	s_lshl_b32 s12, s39, 7
	s_add_i32 m0, s63, 0x18000
	v_lshl_add_u64 v[0:1], v[0:1], 0, s[34:35]
	v_bitop3_b32 v171, v19, s12, v18 bitop3:0xde
	global_load_lds_dwordx4 v[0:1], off
	v_lshl_add_u64 v[0:1], v[2:3], 0, s[34:35]
	s_add_i32 m0, s63, 0x1a000
	s_add_i32 s12, s63, 0x8000
	global_load_lds_dwordx4 v[0:1], off
	v_lshl_add_u64 v[0:1], v[8:9], 0, s[34:35]
	s_mov_b32 m0, s12
	s_add_i32 s19, s63, 0xa000
	global_load_lds_dwordx4 v[0:1], off
	v_lshl_add_u64 v[0:1], v[10:11], 0, s[34:35]
	s_mov_b32 m0, s19
	s_add_i32 s25, s38, s25
	global_load_lds_dwordx4 v[0:1], off
	s_add_i32 m0, s63, 0x1c000
	v_lshl_add_u64 v[0:1], v[4:5], 0, s[34:35]
	global_load_lds_dwordx4 v[0:1], off
	v_lshl_add_u64 v[0:1], v[6:7], 0, s[34:35]
	s_add_i32 m0, s63, 0x1e000
	s_ashr_i32 s25, s25, 6
	global_load_lds_dwordx4 v[0:1], off
	v_add_u32_e32 v0, v14, v12
	s_cmp_gt_i32 s38, 63
	v_add_lshl_u32 v0, v0, v13, 1
	v_mov_b32_e32 v1, v48
	s_waitcnt vmcnt(8)
	s_barrier
	s_waitcnt vmcnt(6)
	s_cselect_b64 s[54:55], -1, 0
	s_add_i32 s69, s25, -2
	v_lshl_add_u64 v[154:155], s[44:45], 0, v[0:1]
	v_add_u32_e32 v0, v17, v15
	s_cmpk_lt_u32 s30, 0x100
	v_add_lshl_u32 v0, v0, v16, 1
	s_cselect_b64 s[56:57], -1, 0
	v_or_b32_e32 v175, s39, v20
	v_lshl_add_u64 v[156:157], s[44:45], 0, v[0:1]
	s_mov_b32 s70, 0
	v_add_u32_e32 v177, 0, v21
	s_barrier
	s_branch .LBB0_1557

.LBB0_1635:
	s_add_u32 s64, s40, 0x18422000
	s_addc_u32 s65, s41, 0
	s_add_i32 m0, s61, 0x18000
	v_lshl_add_u64 v[0:1], v[0:1], 0, s[34:35]
	global_load_lds_dwordx4 v[0:1], off
	v_lshl_add_u64 v[0:1], v[2:3], 0, s[34:35]
	s_add_i32 m0, s61, 0x1a000
	s_add_i32 s79, s61, 0x8000
	global_load_lds_dwordx4 v[0:1], off
	v_lshl_add_u64 v[0:1], v[8:9], 0, s[34:35]
	s_mov_b32 m0, s79
	s_add_i32 s88, s61, 0xa000
	global_load_lds_dwordx4 v[0:1], off
	v_lshl_add_u64 v[0:1], v[10:11], 0, s[34:35]
	s_mov_b32 m0, s88
	v_bfe_u32 v19, v18, 4, 2
	global_load_lds_dwordx4 v[0:1], off
	s_add_i32 m0, s61, 0x1c000
	v_lshl_add_u64 v[0:1], v[4:5], 0, s[34:35]
	global_load_lds_dwordx4 v[0:1], off
	v_lshl_add_u64 v[0:1], v[6:7], 0, s[34:35]
	s_add_i32 m0, s61, 0x1e000
	s_lshr_b32 s39, s39, 26
	global_load_lds_dwordx4 v[0:1], off
	v_lshlrev_b32_e32 v0, 2, v234
	v_and_b32_e32 v0, 60, v0
	v_lshrrev_b32_e32 v1, 4, v234
	v_add_lshl_u32 v181, v0, v1, 2
	v_lshlrev_b32_e32 v0, 3, v234
	v_and_b32_e32 v1, 64, v234
	v_and_b32_e32 v49, 15, v18
	s_add_i32 s39, s38, s39
	v_lshlrev_b32_e32 v20, 4, v19
	v_lshlrev_b32_e32 v18, 2, v18
	v_and_b32_e32 v182, 24, v0
	v_xor_b32_e32 v0, 16, v234
	v_add_u32_e32 v1, 64, v1
	s_and_b32 s40, s42, 3
	s_ashr_i32 s62, s39, 6
	v_lshl_or_b32 v21, v49, 6, v20
	s_lshl_b32 s39, s30, 13
	v_and_b32_e32 v18, 32, v18
	v_cmp_lt_i32_e32 vcc, v0, v1
	s_lshl_b32 s63, s30, 6
	v_bitop3_b32 v22, v21, s39, v18 bitop3:0xde
	s_lshl_b32 s78, s40, 5
	s_lshl_b32 s39, s40, 12
	v_cndmask_b32_e32 v0, v234, v0, vcc
	s_cmp_gt_i32 s38, 63
	v_lshlrev_b32_e32 v183, 2, v0
	v_xor_b32_e32 v0, 32, v234
	s_cselect_b64 s[66:67], -1, 0
	s_add_i32 s89, s62, -2
	v_cmp_lt_i32_e32 vcc, v0, v1
	s_cmpk_lt_u32 s29, 0x100
	s_cselect_b64 s[68:69], -1, 0
	v_cndmask_b32_e32 v0, v234, v0, vcc
	v_lshlrev_b32_e32 v184, 2, v0
	s_lshl_b32 s41, s40, 2
	s_and_b32 s29, s29, 0xffffff00
	s_lshl_b32 s40, s40, 6
	v_add_u32_e32 v0, v14, v12
	s_lshl_b32 s30, s30, 10
	s_or_b32 s29, s40, s29
	v_add_lshl_u32 v0, v0, v13, 1
	v_mov_b32_e32 v1, v48
	s_waitcnt vmcnt(8)
	s_barrier
	s_waitcnt vmcnt(6)
	s_or_b32 s30, s41, s30
	v_or3_b32 v185, s29, v20, v49
	v_lshl_add_u64 v[166:167], s[52:53], 0, v[0:1]
	v_add_u32_e32 v0, v17, v15
	v_lshlrev_b32_e32 v2, 4, v49
	s_add_i32 s30, s30, 0x22400
	s_movk_i32 s29, 0x100
	v_lshlrev_b32_e32 v3, 4, v185
	v_add_lshl_u32 v0, v0, v16, 1
	v_lshlrev_b32_e32 v178, 3, v19
	v_bitop3_b32 v179, v21, s39, v18 bitop3:0xde
	v_lshrrev_b32_e32 v180, 2, v234
	s_mov_b32 s90, 0
	v_cmp_eq_u32_e64 s[38:39], 0, v19
	v_cmp_gt_i32_e64 s[40:41], s29, v185
	v_lshl_add_u64 v[168:169], s[52:53], 0, v[0:1]
	v_add_u32_e32 v186, 0, v22
	v_add_u32_e32 v187, s30, v2
	v_add_u32_e32 v188, 0x22400, v3
	s_barrier
	s_branch .LBB0_1638

.LBB0_1723:
	s_add_u32 s58, s40, 0x18422000
	s_addc_u32 s59, s41, 0
	s_add_u32 s62, s58, s44
	s_addc_u32 s63, s59, s45
	s_add_i32 m0, s25, 0x18000
	v_lshl_add_u64 v[0:1], v[0:1], 0, s[34:35]
	global_load_lds_dwordx4 v[0:1], off
	v_lshl_add_u64 v[0:1], v[2:3], 0, s[34:35]
	s_add_i32 m0, s25, 0x1a000
	s_add_i32 s70, s25, 0x8000
	global_load_lds_dwordx4 v[0:1], off
	v_lshl_add_u64 v[0:1], v[8:9], 0, s[34:35]
	s_mov_b32 m0, s70
	s_add_i32 s71, s25, 0xa000
	global_load_lds_dwordx4 v[0:1], off
	v_lshl_add_u64 v[0:1], v[10:11], 0, s[34:35]
	s_mov_b32 m0, s71
	v_bfe_u32 v19, v18, 4, 2
	global_load_lds_dwordx4 v[0:1], off
	s_add_i32 m0, s25, 0x1c000
	v_lshl_add_u64 v[0:1], v[4:5], 0, s[34:35]
	global_load_lds_dwordx4 v[0:1], off
	v_lshl_add_u64 v[0:1], v[6:7], 0, s[34:35]
	s_add_i32 m0, s25, 0x1e000
	s_and_b32 s40, s30, 3
	global_load_lds_dwordx4 v[0:1], off
	v_and_b32_e32 v49, 15, v18
	s_lshr_b32 s30, s39, 26
	v_lshlrev_b32_e32 v20, 4, v19
	v_lshlrev_b32_e32 v18, 2, v18
	s_add_i32 s30, s38, s30
	v_lshl_or_b32 v21, v49, 6, v20
	s_lshl_b32 s39, s69, 13
	v_and_b32_e32 v18, 32, v18
	s_ashr_i32 s30, s30, 6
	s_lshl_b32 s60, s69, 6
	v_bitop3_b32 v22, v21, s39, v18 bitop3:0xde
	s_lshl_b32 s61, s40, 5
	s_lshl_b32 s39, s40, 12
	s_cmp_gt_i32 s38, 63
	s_cselect_b64 s[64:65], -1, 0
	s_add_i32 s72, s30, -2
	s_cmpk_lt_u32 s68, 0x100
	v_bitop3_b32 v189, v21, s39, v18 bitop3:0xde
	s_cselect_b64 s[66:67], -1, 0
	s_and_b32 s38, s68, 0xffffff00
	s_lshl_b32 s39, s40, 6
	v_lshlrev_b32_e32 v0, 2, v234
	s_or_b32 s38, s39, s38
	v_lshlrev_b32_e32 v2, 3, v234
	v_and_b32_e32 v3, 64, v234
	v_and_b32_e32 v0, 60, v0
	v_lshrrev_b32_e32 v1, 4, v234
	v_or3_b32 v192, s38, v20, v49
	v_and_b32_e32 v193, 24, v2
	v_xor_b32_e32 v2, 16, v234
	v_add_u32_e32 v3, 64, v3
	v_add_lshl_u32 v191, v0, v1, 2
	v_lshlrev_b32_e32 v0, 3, v192
	v_cmp_lt_i32_e32 vcc, v2, v3
	v_ashrrev_i32_e32 v1, 31, v0
	v_lshl_add_u64 v[170:171], v[0:1], 1, s[42:43]
	v_cndmask_b32_e32 v2, v234, v2, vcc
	v_lshlrev_b32_e32 v194, 2, v2
	v_xor_b32_e32 v2, 32, v234
	v_add_u32_e32 v0, v14, v12
	v_cmp_lt_i32_e32 vcc, v2, v3
	s_lshl_b32 s40, s40, 2
	s_lshl_b32 s41, s69, 10
	v_add_lshl_u32 v0, v0, v13, 1
	v_mov_b32_e32 v1, v48
	s_waitcnt vmcnt(8)
	s_barrier
	s_waitcnt vmcnt(6)
	v_cndmask_b32_e32 v2, v234, v2, vcc
	s_or_b32 s40, s40, s41
	v_lshl_add_u64 v[172:173], s[50:51], 0, v[0:1]
	v_add_u32_e32 v0, v17, v15
	v_lshlrev_b32_e32 v195, 2, v2
	v_lshlrev_b32_e32 v2, 4, v49
	s_add_i32 s44, s40, 0x22400
	v_lshlrev_b32_e32 v3, 4, v192
	v_add_lshl_u32 v0, v0, v16, 1
	v_lshlrev_b32_e32 v188, 3, v19
	v_lshrrev_b32_e32 v190, 2, v234
	s_mov_b32 s78, 0
	v_cmp_eq_u32_e64 s[38:39], 0, v19
	v_cmp_gt_i32_e64 s[40:41], s79, v192
	v_lshl_add_u64 v[174:175], s[50:51], 0, v[0:1]
	v_add_u32_e32 v196, 0, v22
	v_add_u32_e32 v197, s44, v2
	v_add_u32_e32 v198, 0x22400, v3
	s_barrier
	s_branch .LBB0_1726

.LBB0_1811:
	s_add_i32 m0, s25, 0x18000
	v_lshl_add_u64 v[0:1], v[0:1], 0, s[34:35]
	global_load_lds_dwordx4 v[0:1], off
	v_lshl_add_u64 v[0:1], v[2:3], 0, s[34:35]
	s_add_i32 m0, s25, 0x1a000
	s_add_i32 s56, s25, 0x8000
	global_load_lds_dwordx4 v[0:1], off
	v_lshl_add_u64 v[0:1], v[8:9], 0, s[34:35]
	s_mov_b32 m0, s56
	s_add_i32 s58, s25, 0xa000
	global_load_lds_dwordx4 v[0:1], off
	v_lshl_add_u64 v[0:1], v[10:11], 0, s[34:35]
	s_mov_b32 m0, s58
	s_and_b32 s51, s30, 3
	global_load_lds_dwordx4 v[0:1], off
	s_add_i32 m0, s25, 0x1c000
	v_lshl_add_u64 v[0:1], v[4:5], 0, s[34:35]
	global_load_lds_dwordx4 v[0:1], off
	v_lshl_add_u64 v[0:1], v[6:7], 0, s[34:35]
	s_add_i32 m0, s25, 0x1e000
	v_and_b32_e32 v19, 15, v17
	global_load_lds_dwordx4 v[0:1], off
	v_and_b32_e32 v20, 48, v17
	s_lshr_b32 s30, s39, 26
	v_lshlrev_b32_e32 v17, 2, v17
	s_add_i32 s30, s38, s30
	v_lshl_or_b32 v21, v19, 6, v20
	s_lshl_b32 s39, s46, 13
	v_and_b32_e32 v17, 32, v17
	s_ashr_i32 s30, s30, 6
	v_bitop3_b32 v22, v21, s39, v17 bitop3:0xde
	s_lshl_b32 s39, s51, 12
	s_cmp_gt_i32 s38, 63
	s_cselect_b64 s[46:47], -1, 0
	s_add_i32 s60, s30, -2
	s_cmpk_lt_u32 s50, 0x100
	v_bitop3_b32 v49, v21, s39, v17 bitop3:0xde
	s_cselect_b64 s[48:49], -1, 0
	s_and_b32 s38, s50, 0x1fffff00
	s_lshl_b32 s39, s51, 6
	s_or_b32 s38, s39, s38
	v_or3_b32 v0, s38, v20, v19
	v_lshlrev_b32_e32 v0, 3, v0
	v_ashrrev_i32_e32 v1, 31, v0
	v_lshl_add_u64 v[138:139], v[0:1], 1, s[40:41]
	v_add_u32_e32 v0, v14, v12
	v_add_lshl_u32 v0, v0, v13, 1
	v_mov_b32_e32 v1, v48
	s_waitcnt vmcnt(8)
	s_barrier
	s_waitcnt vmcnt(6)
	v_lshl_add_u64 v[140:141], s[8:9], 0, v[0:1]
	v_add_u32_e32 v0, v18, v15
	v_add_lshl_u32 v0, v0, v16, 1
	v_lshl_add_u64 v[142:143], s[8:9], 0, v[0:1]
	s_mov_b32 s61, 0
	v_add_u32_e32 v144, 0, v22
	s_barrier
	s_branch .LBB0_1814

.LBB0_1841:
	s_lshl_b64 s[42:43], s[40:41], 11
	s_lshl_b64 s[44:45], s[40:41], 6
	s_add_u32 s58, s48, s42
	s_addc_u32 s59, s49, s43
	s_add_u32 s60, s58, s42
	s_addc_u32 s61, s59, s43
	s_add_u32 s62, s60, s44
	s_addc_u32 s63, s61, s45
	s_add_u32 s42, s62, s44
	s_mul_i32 s30, s40, 0x3c00
	s_addc_u32 s43, s63, s45
	s_mul_hi_i32 s29, s40, 0x3c00
	s_add_u32 s30, s42, s30
	s_mul_hi_i32 s41, s40, 0x180
	s_mulk_i32 s40, 0x180
	s_addc_u32 s29, s43, s29
	s_add_u32 s42, s30, s40
	s_addc_u32 s43, s29, s41
	s_add_i32 m0, s26, 0x18000
	v_lshl_add_u64 v[0:1], v[0:1], 0, s[34:35]
	global_load_lds_dwordx4 v[0:1], off
	v_lshl_add_u64 v[0:1], v[2:3], 0, s[34:35]
	s_add_i32 m0, s26, 0x1a000
	s_add_i32 s92, s26, 0x8000
	global_load_lds_dwordx4 v[0:1], off
	v_lshl_add_u64 v[0:1], v[8:9], 0, s[34:35]
	s_mov_b32 m0, s92
	s_add_i32 s93, s26, 0xa000
	global_load_lds_dwordx4 v[0:1], off
	v_lshl_add_u64 v[0:1], v[10:11], 0, s[34:35]
	s_mov_b32 m0, s93
	v_bfe_u32 v19, v18, 4, 2
	global_load_lds_dwordx4 v[0:1], off
	s_add_i32 m0, s26, 0x1c000
	v_lshl_add_u64 v[0:1], v[4:5], 0, s[34:35]
	global_load_lds_dwordx4 v[0:1], off
	v_lshl_add_u64 v[0:1], v[6:7], 0, s[34:35]
	s_add_i32 m0, s26, 0x1e000
	s_lshr_b32 s29, s39, 26
	global_load_lds_dwordx4 v[0:1], off
	v_and_b32_e32 v49, 15, v18
	s_add_i32 s29, s38, s29
	v_lshlrev_b32_e32 v20, 4, v19
	v_lshlrev_b32_e32 v18, 2, v18
	s_and_b32 s28, s28, 3
	s_ashr_i32 s89, s29, 6
	v_lshl_or_b32 v21, v49, 6, v20
	s_lshl_b32 s29, s25, 13
	v_and_b32_e32 v18, 32, v18
	s_lshl_b32 s90, s25, 6
	v_bitop3_b32 v22, v21, s29, v18 bitop3:0xde
	s_lshl_b32 s91, s28, 5
	s_lshl_b32 s29, s28, 12
	s_cmp_gt_i32 s38, 63
	s_cselect_b64 s[64:65], -1, 0
	s_add_i32 s94, s89, -2
	s_cmpk_lt_u32 s19, 0x100
	v_lshlrev_b32_e32 v0, 2, v234
	v_bitop3_b32 v173, v21, s29, v18 bitop3:0xde
	s_cselect_b64 s[66:67], -1, 0
	v_and_b32_e32 v2, 60, v0
	v_lshrrev_b32_e32 v3, 4, v234
	s_and_b32 s19, s19, 0xffffff00
	s_lshl_b32 s29, s28, 6
	s_or_b32 s19, s29, s19
	v_add_lshl_u32 v191, v2, v3, 2
	v_lshlrev_b32_e32 v2, 3, v234
	v_and_b32_e32 v3, 64, v234
	v_or3_b32 v177, s19, v20, v49
	v_and_b32_e32 v195, 24, v2
	v_xor_b32_e32 v2, 16, v234
	v_add_u32_e32 v3, 64, v3
	v_lshlrev_b32_e32 v0, 3, v177
	v_cmp_lt_i32_e32 vcc, v2, v3
	v_ashrrev_i32_e32 v1, 31, v0
	v_lshl_add_u64 v[162:163], v[0:1], 1, s[42:43]
	v_cndmask_b32_e32 v2, v234, v2, vcc
	v_lshlrev_b32_e32 v199, 2, v2
	v_xor_b32_e32 v2, 32, v234
	v_add_u32_e32 v0, v14, v12
	v_cmp_lt_i32_e32 vcc, v2, v3
	s_lshl_b32 s19, s28, 2
	s_lshl_b32 s25, s25, 10
	v_add_lshl_u32 v0, v0, v13, 1
	v_mov_b32_e32 v1, v48
	s_waitcnt vmcnt(8)
	s_barrier
	s_waitcnt vmcnt(6)
	v_cndmask_b32_e32 v2, v234, v2, vcc
	s_or_b32 s19, s19, s25
	v_lshl_add_u64 v[164:165], s[50:51], 0, v[0:1]
	v_add_u32_e32 v0, v17, v15
	v_lshlrev_b32_e32 v203, 2, v2
	v_lshlrev_b32_e32 v2, 4, v49
	s_add_i32 s19, s19, 0x22400
	v_lshlrev_b32_e32 v3, 4, v177
	v_add_lshl_u32 v0, v0, v16, 1
	v_lshlrev_b32_e32 v169, 3, v19
	v_lshrrev_b32_e32 v187, 2, v234
	s_mov_b32 s95, 0
	v_cmp_eq_u32_e64 s[38:39], 0, v19
	v_cmp_gt_i32_e64 s[40:41], s55, v177
	v_lshl_add_u64 v[166:167], s[50:51], 0, v[0:1]
	v_add_u32_e32 v206, 0, v22
	v_add_u32_e32 v207, s19, v2
	v_add_u32_e32 v208, 0x22400, v3
	s_barrier
	s_branch .LBB0_1844
